# k_l2 fast path at 64 VGPRs / 80 KB LDS / 48 SGPRs so two blocks share a CU (SGPR allocation was capping occupancy); 8000-record LDS tile in two passes
# speedup vs baseline: 1.0690x; 1.0114x over previous
_Z4k_l2PK15HIP_vector_typeIiLj2EEPKiPiPS0_ii:
	s_load_dword s3, s[0:1], 0x28
	s_load_dwordx4 s[36:39], s[0:1], 0x8
	s_load_dwordx2 s[40:41], s[0:1], 0x18
	s_not_b32 s4, s2
	s_waitcnt lgkmcnt(0)
	s_add_i32 s42, s3, s4
	s_ashr_i32 s43, s42, 31
	s_lshl_b64 s[4:5], s[42:43], 2
	s_add_u32 s6, s36, s4
	s_addc_u32 s7, s37, s5
	s_sub_i32 s2, s3, s2
	s_ashr_i32 s3, s2, 31
	s_lshl_b64 s[2:3], s[2:3], 2
	s_add_u32 s2, s36, s2
	s_addc_u32 s3, s37, s3
	s_load_dword s36, s[6:7], 0x0
	s_load_dword s4, s[2:3], 0x0
	s_movk_i32 s2, 0x80
	v_cmp_gt_u32_e64 s[34:35], s2, v0
	s_and_saveexec_b64 s[2:3], s[34:35]
	v_mov_b32_e32 v1, 0x200
	v_lshl_add_u32 v1, v0, 2, v1
	v_mov_b32_e32 v2, 0
	ds_write_b32 v1, v2
	s_or_b64 exec, exec, s[2:3]
	s_load_dwordx2 s[2:3], s[0:1], 0x0
	s_load_dwordx2 s[44:45], s[0:1], 0x20
	s_waitcnt lgkmcnt(0)
	s_sub_i32 s33, s4, s36
	s_cmpk_lt_i32 s33, 0x3e81
	s_mov_b64 s[0:1], -1
	s_barrier
	s_cbranch_scc1 .LBB3_46
	v_add_u32_e32 v2, s36, v0
	v_ashrrev_i32_e32 v3, 31, v2
	v_lshlrev_b64 v[2:3], 3, v[2:3]
	v_lshl_add_u64 v[4:5], s[2:3], 0, v[2:3]
	s_mov_b64 s[0:1], 0
	v_mov_b32_e32 v1, 1
	s_mov_b64 s[4:5], 0x2000
	v_mov_b32_e32 v6, v0
.LBB3_4:
	global_load_dword v7, v[4:5], off
	v_add_u32_e32 v6, 0x400, v6
	v_cmp_le_i32_e32 vcc, s33, v6
	s_or_b64 s[0:1], vcc, s[0:1]
	v_lshl_add_u64 v[4:5], v[4:5], 0, s[4:5]
	s_waitcnt vmcnt(0)
	v_lshrrev_b32_e32 v7, 23, v7
	v_and_b32_e32 v7, 0x1fc, v7
	v_or_b32_e32 v7, 0x200, v7
	ds_add_u32 v7, v1
	s_andn2_b64 exec, exec, s[0:1]
	s_cbranch_execnz .LBB3_4
	s_or_b64 exec, exec, s[0:1]
	v_mov_b32_e32 v6, 0
	v_mov_b32_e32 v4, 0
	s_waitcnt lgkmcnt(0)
	s_barrier
	s_and_saveexec_b64 s[0:1], s[34:35]
	s_cbranch_execz .LBB3_7
	v_lshlrev_b32_e32 v1, 2, v0
	v_add_u32_e32 v4, 0x200, v1
	ds_read_b32 v4, v4
	v_or_b32_e32 v1, 0x0, v1
	s_waitcnt lgkmcnt(0)
	ds_write_b32 v1, v4
.LBB3_7:
	s_or_b64 exec, exec, s[0:1]
	v_mov_b32_e32 v1, 0x0
	s_movk_i32 s0, 0xff80
	v_add_u32_e32 v5, 0xffffff80, v0
	v_lshl_or_b32 v1, v0, 2, v1
	v_cmp_lt_u32_e32 vcc, s0, v5
	s_waitcnt lgkmcnt(0)
	s_barrier
	s_and_saveexec_b64 s[0:1], vcc
	v_add_u32_e32 v6, -4, v1
	ds_read_b32 v6, v6
	s_or_b64 exec, exec, s[0:1]
	s_waitcnt lgkmcnt(0)
	s_barrier
	s_and_saveexec_b64 s[0:1], s[34:35]
	s_cbranch_execz .LBB3_11
	ds_read_b32 v7, v1
	s_waitcnt lgkmcnt(0)
	v_add_u32_e32 v6, v7, v6
	ds_write_b32 v1, v6

.LBB3_44:
	global_load_dwordx2 v[6:7], v[2:3], off offset:-4
	v_add_u32_e32 v4, 0x400, v4
	v_cmp_le_i32_e32 vcc, s33, v4
	v_lshl_add_u64 v[2:3], v[2:3], 0, s[4:5]
	s_or_b64 s[0:1], vcc, s[0:1]
	s_waitcnt vmcnt(0)
	v_lshrrev_b32_e32 v5, 23, v6
	v_and_b32_e32 v5, 0x1fc, v5
	v_or_b32_e32 v5, 0x0, v5
	ds_add_rtn_u32 v8, v5, v1
	v_and_b32_e32 v6, 0x1ffffff, v6
	s_waitcnt lgkmcnt(0)
	v_ashrrev_i32_e32 v9, 31, v8
	v_lshl_add_u64 v[8:9], v[8:9], 3, s[40:41]
	global_store_dwordx2 v[8:9], v[6:7], off
	s_andn2_b64 exec, exec, s[0:1]
	s_cbranch_execnz .LBB3_44
	s_or_b64 exec, exec, s[0:1]
	s_mov_b64 s[0:1], 0
.LBB3_46:
	s_and_b64 vcc, exec, s[0:1]
	s_cbranch_vccz .LBB3_141
	s_ashr_i32 s37, s36, 31
	s_lshl_b64 s[0:1], s[36:37], 3
	s_add_u32 s0, s2, s0
	s_addc_u32 s1, s3, s1
	s_add_i32 s8, s44, 31
	s_lshr_b32 s8, s8, 5
	s_add_i32 s8, s8, -1
	s_lshl_b32 s9, s42, 2
	s_sub_i32 s8, s8, s9
	s_bfe_u32 s8, s8, 0x1000a
	s_mul_i32 s8, s8, 31
	v_mov_b32_e32 v50, 0
	v_mov_b32_e32 v51, 0
	v_mov_b32_e32 v52, 0
	v_mov_b32_e32 v53, 0
	v_lshlrev_b32_e32 v1, 4, v0
	ds_write_b128 v1, v[50:53]
	v_mov_b32_e32 v63, 1
	v_add_u32_e32 v54, 0, v0
	v_lshl_add_u32 v54, v54, 1, 0
	v_cmp_gt_i32_e32 vcc, s33, v54
	v_lshlrev_b32_e32 v54, 3, v54
	s_and_saveexec_b64 s[4:5], vcc
	global_load_dwordx4 v[2:5], v54, s[0:1] nt
	s_or_b64 exec, exec, s[4:5]
	v_add_u32_e32 v54, 1024, v0
	v_lshl_add_u32 v54, v54, 1, 0
	v_cmp_gt_i32_e32 vcc, s33, v54
	v_lshlrev_b32_e32 v54, 3, v54
	s_and_saveexec_b64 s[4:5], vcc
	global_load_dwordx4 v[6:9], v54, s[0:1] nt
	s_or_b64 exec, exec, s[4:5]
	v_add_u32_e32 v54, 2048, v0
	v_lshl_add_u32 v54, v54, 1, 0
	v_cmp_gt_i32_e32 vcc, s33, v54
	v_lshlrev_b32_e32 v54, 3, v54
	s_and_saveexec_b64 s[4:5], vcc
	global_load_dwordx4 v[10:13], v54, s[0:1] nt
	s_or_b64 exec, exec, s[4:5]
	v_add_u32_e32 v54, 3072, v0
	v_lshl_add_u32 v54, v54, 1, 0
	v_cmp_gt_i32_e32 vcc, s33, v54
	v_lshlrev_b32_e32 v54, 3, v54
	s_and_saveexec_b64 s[4:5], vcc
	global_load_dwordx4 v[14:17], v54, s[0:1] nt
	s_or_b64 exec, exec, s[4:5]
	v_add_u32_e32 v54, 4096, v0
	v_lshl_add_u32 v54, v54, 1, 0
	v_cmp_gt_i32_e32 vcc, s33, v54
	v_lshlrev_b32_e32 v54, 3, v54
	s_and_saveexec_b64 s[4:5], vcc
	global_load_dwordx4 v[18:21], v54, s[0:1] nt
	s_or_b64 exec, exec, s[4:5]
	v_add_u32_e32 v54, 5120, v0
	v_lshl_add_u32 v54, v54, 1, 0
	v_cmp_gt_i32_e32 vcc, s33, v54
	v_lshlrev_b32_e32 v54, 3, v54
	s_and_saveexec_b64 s[4:5], vcc
	global_load_dwordx4 v[22:25], v54, s[0:1] nt
	s_or_b64 exec, exec, s[4:5]
	v_add_u32_e32 v54, 6144, v0
	v_lshl_add_u32 v54, v54, 1, 0
	v_cmp_gt_i32_e32 vcc, s33, v54
	v_lshlrev_b32_e32 v54, 3, v54
	s_and_saveexec_b64 s[4:5], vcc
	global_load_dwordx4 v[26:29], v54, s[0:1] nt
	s_or_b64 exec, exec, s[4:5]
	v_add_u32_e32 v54, 7168, v0
	v_lshl_add_u32 v54, v54, 1, 0
	v_cmp_gt_i32_e32 vcc, s33, v54
	v_lshlrev_b32_e32 v54, 3, v54
	s_and_saveexec_b64 s[4:5], vcc
	global_load_dwordx4 v[30:33], v54, s[0:1] nt
	s_or_b64 exec, exec, s[4:5]
	s_waitcnt lgkmcnt(0)
	s_barrier
	s_waitcnt vmcnt(7)
	v_lshrrev_b32_e32 v54, 25, v2
	v_bfe_u32 v55, v2, 13, 12
	v_min_u32_e32 v55, 31, v55
	v_xor_b32_e32 v55, s8, v55
	v_lshl_or_b32 v54, v54, 5, v55
	v_lshlrev_b32_e32 v56, 2, v54
	v_add_u32_e32 v54, 0, v0
	v_lshl_add_u32 v54, v54, 1, 0
	v_cmp_gt_i32_e32 vcc, s33, v54
	s_and_saveexec_b64 s[4:5], vcc
	ds_add_rtn_u32 v34, v56, v63
	s_or_b64 exec, exec, s[4:5]
	s_waitcnt vmcnt(7)
	v_lshrrev_b32_e32 v54, 25, v4
	v_bfe_u32 v55, v4, 13, 12
	v_min_u32_e32 v55, 31, v55
	v_xor_b32_e32 v55, s8, v55
	v_lshl_or_b32 v54, v54, 5, v55
	v_lshlrev_b32_e32 v56, 2, v54
	v_add_u32_e32 v54, 0, v0
	v_lshl_add_u32 v54, v54, 1, 1
	v_cmp_gt_i32_e32 vcc, s33, v54
	s_and_saveexec_b64 s[4:5], vcc
	ds_add_rtn_u32 v35, v56, v63
	s_or_b64 exec, exec, s[4:5]
	s_waitcnt vmcnt(6)
	v_lshrrev_b32_e32 v54, 25, v6
	v_bfe_u32 v55, v6, 13, 12
	v_min_u32_e32 v55, 31, v55
	v_xor_b32_e32 v55, s8, v55
	v_lshl_or_b32 v54, v54, 5, v55
	v_lshlrev_b32_e32 v56, 2, v54
	v_add_u32_e32 v54, 1024, v0
	v_lshl_add_u32 v54, v54, 1, 0
	v_cmp_gt_i32_e32 vcc, s33, v54
	s_and_saveexec_b64 s[4:5], vcc
	ds_add_rtn_u32 v36, v56, v63
	s_or_b64 exec, exec, s[4:5]
	s_waitcnt vmcnt(6)
	v_lshrrev_b32_e32 v54, 25, v8
	v_bfe_u32 v55, v8, 13, 12
	v_min_u32_e32 v55, 31, v55
	v_xor_b32_e32 v55, s8, v55
	v_lshl_or_b32 v54, v54, 5, v55
	v_lshlrev_b32_e32 v56, 2, v54
	v_add_u32_e32 v54, 1024, v0
	v_lshl_add_u32 v54, v54, 1, 1
	v_cmp_gt_i32_e32 vcc, s33, v54
	s_and_saveexec_b64 s[4:5], vcc
	ds_add_rtn_u32 v37, v56, v63
	s_or_b64 exec, exec, s[4:5]
	s_waitcnt vmcnt(5)
	v_lshrrev_b32_e32 v54, 25, v10
	v_bfe_u32 v55, v10, 13, 12
	v_min_u32_e32 v55, 31, v55
	v_xor_b32_e32 v55, s8, v55
	v_lshl_or_b32 v54, v54, 5, v55
	v_lshlrev_b32_e32 v56, 2, v54
	v_add_u32_e32 v54, 2048, v0
	v_lshl_add_u32 v54, v54, 1, 0
	v_cmp_gt_i32_e32 vcc, s33, v54
	s_and_saveexec_b64 s[4:5], vcc
	ds_add_rtn_u32 v38, v56, v63
	s_or_b64 exec, exec, s[4:5]
	s_waitcnt vmcnt(5)
	v_lshrrev_b32_e32 v54, 25, v12
	v_bfe_u32 v55, v12, 13, 12
	v_min_u32_e32 v55, 31, v55
	v_xor_b32_e32 v55, s8, v55
	v_lshl_or_b32 v54, v54, 5, v55
	v_lshlrev_b32_e32 v56, 2, v54
	v_add_u32_e32 v54, 2048, v0
	v_lshl_add_u32 v54, v54, 1, 1
	v_cmp_gt_i32_e32 vcc, s33, v54
	s_and_saveexec_b64 s[4:5], vcc
	ds_add_rtn_u32 v39, v56, v63
	s_or_b64 exec, exec, s[4:5]
	s_waitcnt vmcnt(4)
	v_lshrrev_b32_e32 v54, 25, v14
	v_bfe_u32 v55, v14, 13, 12
	v_min_u32_e32 v55, 31, v55
	v_xor_b32_e32 v55, s8, v55
	v_lshl_or_b32 v54, v54, 5, v55
	v_lshlrev_b32_e32 v56, 2, v54
	v_add_u32_e32 v54, 3072, v0
	v_lshl_add_u32 v54, v54, 1, 0
	v_cmp_gt_i32_e32 vcc, s33, v54
	s_and_saveexec_b64 s[4:5], vcc
	ds_add_rtn_u32 v40, v56, v63
	s_or_b64 exec, exec, s[4:5]
	s_waitcnt vmcnt(4)
	v_lshrrev_b32_e32 v54, 25, v16
	v_bfe_u32 v55, v16, 13, 12
	v_min_u32_e32 v55, 31, v55
	v_xor_b32_e32 v55, s8, v55
	v_lshl_or_b32 v54, v54, 5, v55
	v_lshlrev_b32_e32 v56, 2, v54
	v_add_u32_e32 v54, 3072, v0
	v_lshl_add_u32 v54, v54, 1, 1
	v_cmp_gt_i32_e32 vcc, s33, v54
	s_and_saveexec_b64 s[4:5], vcc
	ds_add_rtn_u32 v41, v56, v63
	s_or_b64 exec, exec, s[4:5]
	s_waitcnt vmcnt(3)
	v_lshrrev_b32_e32 v54, 25, v18
	v_bfe_u32 v55, v18, 13, 12
	v_min_u32_e32 v55, 31, v55
	v_xor_b32_e32 v55, s8, v55
	v_lshl_or_b32 v54, v54, 5, v55
	v_lshlrev_b32_e32 v56, 2, v54
	v_add_u32_e32 v54, 4096, v0
	v_lshl_add_u32 v54, v54, 1, 0
	v_cmp_gt_i32_e32 vcc, s33, v54
	s_and_saveexec_b64 s[4:5], vcc
	ds_add_rtn_u32 v42, v56, v63
	s_or_b64 exec, exec, s[4:5]
	s_waitcnt vmcnt(3)
	v_lshrrev_b32_e32 v54, 25, v20
	v_bfe_u32 v55, v20, 13, 12
	v_min_u32_e32 v55, 31, v55
	v_xor_b32_e32 v55, s8, v55
	v_lshl_or_b32 v54, v54, 5, v55
	v_lshlrev_b32_e32 v56, 2, v54
	v_add_u32_e32 v54, 4096, v0
	v_lshl_add_u32 v54, v54, 1, 1
	v_cmp_gt_i32_e32 vcc, s33, v54
	s_and_saveexec_b64 s[4:5], vcc
	ds_add_rtn_u32 v43, v56, v63
	s_or_b64 exec, exec, s[4:5]
	s_waitcnt vmcnt(2)
	v_lshrrev_b32_e32 v54, 25, v22
	v_bfe_u32 v55, v22, 13, 12
	v_min_u32_e32 v55, 31, v55
	v_xor_b32_e32 v55, s8, v55
	v_lshl_or_b32 v54, v54, 5, v55
	v_lshlrev_b32_e32 v56, 2, v54
	v_add_u32_e32 v54, 5120, v0
	v_lshl_add_u32 v54, v54, 1, 0
	v_cmp_gt_i32_e32 vcc, s33, v54
	s_and_saveexec_b64 s[4:5], vcc
	ds_add_rtn_u32 v44, v56, v63
	s_or_b64 exec, exec, s[4:5]
	s_waitcnt vmcnt(2)
	v_lshrrev_b32_e32 v54, 25, v24
	v_bfe_u32 v55, v24, 13, 12
	v_min_u32_e32 v55, 31, v55
	v_xor_b32_e32 v55, s8, v55
	v_lshl_or_b32 v54, v54, 5, v55
	v_lshlrev_b32_e32 v56, 2, v54
	v_add_u32_e32 v54, 5120, v0
	v_lshl_add_u32 v54, v54, 1, 1
	v_cmp_gt_i32_e32 vcc, s33, v54
	s_and_saveexec_b64 s[4:5], vcc
	ds_add_rtn_u32 v45, v56, v63
	s_or_b64 exec, exec, s[4:5]
	s_waitcnt vmcnt(1)
	v_lshrrev_b32_e32 v54, 25, v26
	v_bfe_u32 v55, v26, 13, 12
	v_min_u32_e32 v55, 31, v55
	v_xor_b32_e32 v55, s8, v55
	v_lshl_or_b32 v54, v54, 5, v55
	v_lshlrev_b32_e32 v56, 2, v54
	v_add_u32_e32 v54, 6144, v0
	v_lshl_add_u32 v54, v54, 1, 0
	v_cmp_gt_i32_e32 vcc, s33, v54
	s_and_saveexec_b64 s[4:5], vcc
	ds_add_rtn_u32 v46, v56, v63
	s_or_b64 exec, exec, s[4:5]
	s_waitcnt vmcnt(1)
	v_lshrrev_b32_e32 v54, 25, v28
	v_bfe_u32 v55, v28, 13, 12
	v_min_u32_e32 v55, 31, v55
	v_xor_b32_e32 v55, s8, v55
	v_lshl_or_b32 v54, v54, 5, v55
	v_lshlrev_b32_e32 v56, 2, v54
	v_add_u32_e32 v54, 6144, v0
	v_lshl_add_u32 v54, v54, 1, 1
	v_cmp_gt_i32_e32 vcc, s33, v54
	s_and_saveexec_b64 s[4:5], vcc
	ds_add_rtn_u32 v47, v56, v63
	s_or_b64 exec, exec, s[4:5]
	s_waitcnt vmcnt(0)
	v_lshrrev_b32_e32 v54, 25, v30
	v_bfe_u32 v55, v30, 13, 12
	v_min_u32_e32 v55, 31, v55
	v_xor_b32_e32 v55, s8, v55
	v_lshl_or_b32 v54, v54, 5, v55
	v_lshlrev_b32_e32 v56, 2, v54
	v_add_u32_e32 v54, 7168, v0
	v_lshl_add_u32 v54, v54, 1, 0
	v_cmp_gt_i32_e32 vcc, s33, v54
	s_and_saveexec_b64 s[4:5], vcc
	ds_add_rtn_u32 v48, v56, v63
	s_or_b64 exec, exec, s[4:5]
	s_waitcnt vmcnt(0)
	v_lshrrev_b32_e32 v54, 25, v32
	v_bfe_u32 v55, v32, 13, 12
	v_min_u32_e32 v55, 31, v55
	v_xor_b32_e32 v55, s8, v55
	v_lshl_or_b32 v54, v54, 5, v55
	v_lshlrev_b32_e32 v56, 2, v54
	v_add_u32_e32 v54, 7168, v0
	v_lshl_add_u32 v54, v54, 1, 1
	v_cmp_gt_i32_e32 vcc, s33, v54
	s_and_saveexec_b64 s[4:5], vcc
	ds_add_rtn_u32 v49, v56, v63
	s_or_b64 exec, exec, s[4:5]
	s_waitcnt lgkmcnt(0)
	s_barrier
	ds_read_b128 v[50:53], v1
	v_mbcnt_lo_u32_b32 v54, -1, 0
	v_mbcnt_hi_u32_b32 v54, -1, v54
	v_lshrrev_b32_e32 v55, 6, v0
	s_waitcnt lgkmcnt(0)
	v_add_u32_e32 v56, v50, v51
	v_add_u32_e32 v57, v56, v52
	v_add_u32_e32 v58, v57, v53
	v_mov_b32_e32 v59, v58
	v_subrev_u32_e32 v61, 1, v54
	v_lshlrev_b32_e32 v61, 2, v61
	ds_bpermute_b32 v60, v61, v59
	v_cmp_le_u32_e32 vcc, 1, v54
	s_waitcnt lgkmcnt(0)
	v_cndmask_b32_e32 v60, 0, v60, vcc
	v_add_u32_e32 v59, v59, v60
	v_subrev_u32_e32 v61, 2, v54
	v_lshlrev_b32_e32 v61, 2, v61
	ds_bpermute_b32 v60, v61, v59
	v_cmp_le_u32_e32 vcc, 2, v54
	s_waitcnt lgkmcnt(0)
	v_cndmask_b32_e32 v60, 0, v60, vcc
	v_add_u32_e32 v59, v59, v60
	v_subrev_u32_e32 v61, 4, v54
	v_lshlrev_b32_e32 v61, 2, v61
	ds_bpermute_b32 v60, v61, v59
	v_cmp_le_u32_e32 vcc, 4, v54
	s_waitcnt lgkmcnt(0)
	v_cndmask_b32_e32 v60, 0, v60, vcc
	v_add_u32_e32 v59, v59, v60
	v_subrev_u32_e32 v61, 8, v54
	v_lshlrev_b32_e32 v61, 2, v61
	ds_bpermute_b32 v60, v61, v59
	v_cmp_le_u32_e32 vcc, 8, v54
	s_waitcnt lgkmcnt(0)
	v_cndmask_b32_e32 v60, 0, v60, vcc
	v_add_u32_e32 v59, v59, v60
	v_subrev_u32_e32 v61, 16, v54
	v_lshlrev_b32_e32 v61, 2, v61
	ds_bpermute_b32 v60, v61, v59
	v_cmp_le_u32_e32 vcc, 16, v54
	s_waitcnt lgkmcnt(0)
	v_cndmask_b32_e32 v60, 0, v60, vcc
	v_add_u32_e32 v59, v59, v60
	v_subrev_u32_e32 v61, 32, v54
	v_lshlrev_b32_e32 v61, 2, v61
	ds_bpermute_b32 v60, v61, v59
	v_cmp_le_u32_e32 vcc, 32, v54
	s_waitcnt lgkmcnt(0)
	v_cndmask_b32_e32 v60, 0, v60, vcc
	v_add_u32_e32 v59, v59, v60
	v_lshlrev_b32_e32 v61, 2, v55
	v_cmp_eq_u32_e32 vcc, 63, v54
	s_and_saveexec_b64 s[4:5], vcc
	ds_write_b32 v61, v59 offset:16384
	s_or_b64 exec, exec, s[4:5]
	s_waitcnt lgkmcnt(0)
	s_barrier
	v_mov_b32_e32 v54, 0
	v_mov_b32_e32 v61, 0
	ds_read_b128 v[60:63], v61 offset:16384
	s_waitcnt lgkmcnt(0)
	v_cmp_lt_u32_e32 vcc, 0, v55
	s_nop 1
	v_cndmask_b32_e32 v60, 0, v60, vcc
	v_add_u32_e32 v54, v54, v60
	v_cmp_lt_u32_e32 vcc, 1, v55
	s_nop 1
	v_cndmask_b32_e32 v61, 0, v61, vcc
	v_add_u32_e32 v54, v54, v61
	v_cmp_lt_u32_e32 vcc, 2, v55
	s_nop 1
	v_cndmask_b32_e32 v62, 0, v62, vcc
	v_add_u32_e32 v54, v54, v62
	v_cmp_lt_u32_e32 vcc, 3, v55
	s_nop 1
	v_cndmask_b32_e32 v63, 0, v63, vcc
	v_add_u32_e32 v54, v54, v63
	v_mov_b32_e32 v61, 0
	ds_read_b128 v[60:63], v61 offset:16400
	s_waitcnt lgkmcnt(0)
	v_cmp_lt_u32_e32 vcc, 4, v55
	s_nop 1
	v_cndmask_b32_e32 v60, 0, v60, vcc
	v_add_u32_e32 v54, v54, v60
	v_cmp_lt_u32_e32 vcc, 5, v55
	s_nop 1
	v_cndmask_b32_e32 v61, 0, v61, vcc
	v_add_u32_e32 v54, v54, v61
	v_cmp_lt_u32_e32 vcc, 6, v55
	s_nop 1
	v_cndmask_b32_e32 v62, 0, v62, vcc
	v_add_u32_e32 v54, v54, v62
	v_cmp_lt_u32_e32 vcc, 7, v55
	s_nop 1
	v_cndmask_b32_e32 v63, 0, v63, vcc
	v_add_u32_e32 v54, v54, v63
	v_mov_b32_e32 v61, 0
	ds_read_b128 v[60:63], v61 offset:16416
	s_waitcnt lgkmcnt(0)
	v_cmp_lt_u32_e32 vcc, 8, v55
	s_nop 1
	v_cndmask_b32_e32 v60, 0, v60, vcc
	v_add_u32_e32 v54, v54, v60
	v_cmp_lt_u32_e32 vcc, 9, v55
	s_nop 1
	v_cndmask_b32_e32 v61, 0, v61, vcc
	v_add_u32_e32 v54, v54, v61
	v_cmp_lt_u32_e32 vcc, 10, v55
	s_nop 1
	v_cndmask_b32_e32 v62, 0, v62, vcc
	v_add_u32_e32 v54, v54, v62
	v_cmp_lt_u32_e32 vcc, 11, v55
	s_nop 1
	v_cndmask_b32_e32 v63, 0, v63, vcc
	v_add_u32_e32 v54, v54, v63
	v_mov_b32_e32 v61, 0
	ds_read_b128 v[60:63], v61 offset:16432
	s_waitcnt lgkmcnt(0)
	v_cmp_lt_u32_e32 vcc, 12, v55
	s_nop 1
	v_cndmask_b32_e32 v60, 0, v60, vcc
	v_add_u32_e32 v54, v54, v60
	v_cmp_lt_u32_e32 vcc, 13, v55
	s_nop 1
	v_cndmask_b32_e32 v61, 0, v61, vcc
	v_add_u32_e32 v54, v54, v61
	v_cmp_lt_u32_e32 vcc, 14, v55
	s_nop 1
	v_cndmask_b32_e32 v62, 0, v62, vcc
	v_add_u32_e32 v54, v54, v62
	v_mov_b32_e32 v62, v54
	v_sub_u32_e32 v59, v59, v58
	v_add_u32_e32 v59, v59, v62
	v_add_u32_e32 v60, v59, v50
	v_add_u32_e32 v61, v59, v56
	v_add_u32_e32 v62, v59, v57
	v_mov_b32_e32 v50, v59
	v_mov_b32_e32 v51, v60
	v_mov_b32_e32 v52, v61
	v_mov_b32_e32 v53, v62
	ds_write_b128 v1, v[50:53]
	v_and_b32_e32 v56, 7, v0
	v_lshrrev_b32_e32 v57, 3, v0
	v_lshl_add_u32 v57, s42, 7, v57
	v_cmp_eq_u32_e32 vcc, 0, v56
	v_cmp_gt_i32_e64 s[4:5], s44, v57
	s_and_b64 s[4:5], vcc, s[4:5]
	v_add_u32_e32 v58, s36, v59
	v_lshlrev_b32_e32 v56, 2, v57
	s_and_saveexec_b64 s[10:11], s[4:5]
	global_store_dword v56, v58, s[38:39]
	s_add_i32 s7, s44, -1
	v_cmp_eq_u32_e32 vcc, s7, v57
	s_and_b64 exec, exec, vcc
	v_mov_b32_e32 v58, s45
	global_store_dword v56, v58, s[38:39] offset:4
	s_mov_b64 exec, s[10:11]
	s_waitcnt lgkmcnt(0)
	s_barrier
	v_lshrrev_b32_e32 v54, 25, v2
	v_bfe_u32 v55, v2, 13, 12
	v_min_u32_e32 v55, 31, v55
	v_xor_b32_e32 v55, s8, v55
	v_lshl_or_b32 v54, v54, 5, v55
	v_lshlrev_b32_e32 v56, 2, v54
	ds_read_b32 v56, v56
	v_lshrrev_b32_e32 v54, 25, v4
	v_bfe_u32 v55, v4, 13, 12
	v_min_u32_e32 v55, 31, v55
	v_xor_b32_e32 v55, s8, v55
	v_lshl_or_b32 v54, v54, 5, v55
	v_lshlrev_b32_e32 v57, 2, v54
	ds_read_b32 v57, v57
	v_lshrrev_b32_e32 v54, 25, v6
	v_bfe_u32 v55, v6, 13, 12
	v_min_u32_e32 v55, 31, v55
	v_xor_b32_e32 v55, s8, v55
	v_lshl_or_b32 v54, v54, 5, v55
	v_lshlrev_b32_e32 v58, 2, v54
	ds_read_b32 v58, v58
	v_lshrrev_b32_e32 v54, 25, v8
	v_bfe_u32 v55, v8, 13, 12
	v_min_u32_e32 v55, 31, v55
	v_xor_b32_e32 v55, s8, v55
	v_lshl_or_b32 v54, v54, 5, v55
	v_lshlrev_b32_e32 v59, 2, v54
	ds_read_b32 v59, v59
	s_waitcnt lgkmcnt(0)
	v_add_u32_e32 v34, v34, v56
	v_and_b32_e32 v2, 0x1ffffff, v2
	v_add_u32_e32 v35, v35, v57
	v_and_b32_e32 v4, 0x1ffffff, v4
	v_add_u32_e32 v36, v36, v58
	v_and_b32_e32 v6, 0x1ffffff, v6
	v_add_u32_e32 v37, v37, v59
	v_and_b32_e32 v8, 0x1ffffff, v8
	v_lshrrev_b32_e32 v54, 25, v10
	v_bfe_u32 v55, v10, 13, 12
	v_min_u32_e32 v55, 31, v55
	v_xor_b32_e32 v55, s8, v55
	v_lshl_or_b32 v54, v54, 5, v55
	v_lshlrev_b32_e32 v56, 2, v54
	ds_read_b32 v56, v56
	v_lshrrev_b32_e32 v54, 25, v12
	v_bfe_u32 v55, v12, 13, 12
	v_min_u32_e32 v55, 31, v55
	v_xor_b32_e32 v55, s8, v55
	v_lshl_or_b32 v54, v54, 5, v55
	v_lshlrev_b32_e32 v57, 2, v54
	ds_read_b32 v57, v57
	v_lshrrev_b32_e32 v54, 25, v14
	v_bfe_u32 v55, v14, 13, 12
	v_min_u32_e32 v55, 31, v55
	v_xor_b32_e32 v55, s8, v55
	v_lshl_or_b32 v54, v54, 5, v55
	v_lshlrev_b32_e32 v58, 2, v54
	ds_read_b32 v58, v58
	v_lshrrev_b32_e32 v54, 25, v16
	v_bfe_u32 v55, v16, 13, 12
	v_min_u32_e32 v55, 31, v55
	v_xor_b32_e32 v55, s8, v55
	v_lshl_or_b32 v54, v54, 5, v55
	v_lshlrev_b32_e32 v59, 2, v54
	ds_read_b32 v59, v59
	s_waitcnt lgkmcnt(0)
	v_add_u32_e32 v38, v38, v56
	v_and_b32_e32 v10, 0x1ffffff, v10
	v_add_u32_e32 v39, v39, v57
	v_and_b32_e32 v12, 0x1ffffff, v12
	v_add_u32_e32 v40, v40, v58
	v_and_b32_e32 v14, 0x1ffffff, v14
	v_add_u32_e32 v41, v41, v59
	v_and_b32_e32 v16, 0x1ffffff, v16
	v_lshrrev_b32_e32 v54, 25, v18
	v_bfe_u32 v55, v18, 13, 12
	v_min_u32_e32 v55, 31, v55
	v_xor_b32_e32 v55, s8, v55
	v_lshl_or_b32 v54, v54, 5, v55
	v_lshlrev_b32_e32 v56, 2, v54
	ds_read_b32 v56, v56
	v_lshrrev_b32_e32 v54, 25, v20
	v_bfe_u32 v55, v20, 13, 12
	v_min_u32_e32 v55, 31, v55
	v_xor_b32_e32 v55, s8, v55
	v_lshl_or_b32 v54, v54, 5, v55
	v_lshlrev_b32_e32 v57, 2, v54
	ds_read_b32 v57, v57
	v_lshrrev_b32_e32 v54, 25, v22
	v_bfe_u32 v55, v22, 13, 12
	v_min_u32_e32 v55, 31, v55
	v_xor_b32_e32 v55, s8, v55
	v_lshl_or_b32 v54, v54, 5, v55
	v_lshlrev_b32_e32 v58, 2, v54
	ds_read_b32 v58, v58
	v_lshrrev_b32_e32 v54, 25, v24
	v_bfe_u32 v55, v24, 13, 12
	v_min_u32_e32 v55, 31, v55
	v_xor_b32_e32 v55, s8, v55
	v_lshl_or_b32 v54, v54, 5, v55
	v_lshlrev_b32_e32 v59, 2, v54
	ds_read_b32 v59, v59
	s_waitcnt lgkmcnt(0)
	v_add_u32_e32 v42, v42, v56
	v_and_b32_e32 v18, 0x1ffffff, v18
	v_add_u32_e32 v43, v43, v57
	v_and_b32_e32 v20, 0x1ffffff, v20
	v_add_u32_e32 v44, v44, v58
	v_and_b32_e32 v22, 0x1ffffff, v22
	v_add_u32_e32 v45, v45, v59
	v_and_b32_e32 v24, 0x1ffffff, v24
	v_lshrrev_b32_e32 v54, 25, v26
	v_bfe_u32 v55, v26, 13, 12
	v_min_u32_e32 v55, 31, v55
	v_xor_b32_e32 v55, s8, v55
	v_lshl_or_b32 v54, v54, 5, v55
	v_lshlrev_b32_e32 v56, 2, v54
	ds_read_b32 v56, v56
	v_lshrrev_b32_e32 v54, 25, v28
	v_bfe_u32 v55, v28, 13, 12
	v_min_u32_e32 v55, 31, v55
	v_xor_b32_e32 v55, s8, v55
	v_lshl_or_b32 v54, v54, 5, v55
	v_lshlrev_b32_e32 v57, 2, v54
	ds_read_b32 v57, v57
	v_lshrrev_b32_e32 v54, 25, v30
	v_bfe_u32 v55, v30, 13, 12
	v_min_u32_e32 v55, 31, v55
	v_xor_b32_e32 v55, s8, v55
	v_lshl_or_b32 v54, v54, 5, v55
	v_lshlrev_b32_e32 v58, 2, v54
	ds_read_b32 v58, v58
	v_lshrrev_b32_e32 v54, 25, v32
	v_bfe_u32 v55, v32, 13, 12
	v_min_u32_e32 v55, 31, v55
	v_xor_b32_e32 v55, s8, v55
	v_lshl_or_b32 v54, v54, 5, v55
	v_lshlrev_b32_e32 v59, 2, v54
	ds_read_b32 v59, v59
	s_waitcnt lgkmcnt(0)
	v_add_u32_e32 v46, v46, v56
	v_and_b32_e32 v26, 0x1ffffff, v26
	v_add_u32_e32 v47, v47, v57
	v_and_b32_e32 v28, 0x1ffffff, v28
	v_add_u32_e32 v48, v48, v58
	v_and_b32_e32 v30, 0x1ffffff, v30
	v_add_u32_e32 v49, v49, v59
	v_and_b32_e32 v32, 0x1ffffff, v32
	s_movk_i32 s14, 8000
	v_add_u32_e32 v54, 0, v0
	v_lshl_add_u32 v54, v54, 1, 0
	v_cmp_gt_i32_e32 vcc, s33, v54
	v_mov_b32_e32 v56, v34
	v_cmp_gt_u32_e64 s[4:5], s14, v56
	s_and_b64 vcc, vcc, s[4:5]
	v_lshlrev_b32_e32 v56, 3, v56
	s_and_saveexec_b64 s[4:5], vcc
	ds_write_b64 v56, v[2:3] offset:16448
	s_or_b64 exec, exec, s[4:5]
	v_add_u32_e32 v54, 0, v0
	v_lshl_add_u32 v54, v54, 1, 1
	v_cmp_gt_i32_e32 vcc, s33, v54
	v_mov_b32_e32 v56, v35
	v_cmp_gt_u32_e64 s[4:5], s14, v56
	s_and_b64 vcc, vcc, s[4:5]
	v_lshlrev_b32_e32 v56, 3, v56
	s_and_saveexec_b64 s[4:5], vcc
	ds_write_b64 v56, v[4:5] offset:16448
	s_or_b64 exec, exec, s[4:5]
	v_add_u32_e32 v54, 1024, v0
	v_lshl_add_u32 v54, v54, 1, 0
	v_cmp_gt_i32_e32 vcc, s33, v54
	v_mov_b32_e32 v56, v36
	v_cmp_gt_u32_e64 s[4:5], s14, v56
	s_and_b64 vcc, vcc, s[4:5]
	v_lshlrev_b32_e32 v56, 3, v56
	s_and_saveexec_b64 s[4:5], vcc
	ds_write_b64 v56, v[6:7] offset:16448
	s_or_b64 exec, exec, s[4:5]
	v_add_u32_e32 v54, 1024, v0
	v_lshl_add_u32 v54, v54, 1, 1
	v_cmp_gt_i32_e32 vcc, s33, v54
	v_mov_b32_e32 v56, v37
	v_cmp_gt_u32_e64 s[4:5], s14, v56
	s_and_b64 vcc, vcc, s[4:5]
	v_lshlrev_b32_e32 v56, 3, v56
	s_and_saveexec_b64 s[4:5], vcc
	ds_write_b64 v56, v[8:9] offset:16448
	s_or_b64 exec, exec, s[4:5]
	v_add_u32_e32 v54, 2048, v0
	v_lshl_add_u32 v54, v54, 1, 0
	v_cmp_gt_i32_e32 vcc, s33, v54
	v_mov_b32_e32 v56, v38
	v_cmp_gt_u32_e64 s[4:5], s14, v56
	s_and_b64 vcc, vcc, s[4:5]
	v_lshlrev_b32_e32 v56, 3, v56
	s_and_saveexec_b64 s[4:5], vcc
	ds_write_b64 v56, v[10:11] offset:16448
	s_or_b64 exec, exec, s[4:5]
	v_add_u32_e32 v54, 2048, v0
	v_lshl_add_u32 v54, v54, 1, 1
	v_cmp_gt_i32_e32 vcc, s33, v54
	v_mov_b32_e32 v56, v39
	v_cmp_gt_u32_e64 s[4:5], s14, v56
	s_and_b64 vcc, vcc, s[4:5]
	v_lshlrev_b32_e32 v56, 3, v56
	s_and_saveexec_b64 s[4:5], vcc
	ds_write_b64 v56, v[12:13] offset:16448
	s_or_b64 exec, exec, s[4:5]
	v_add_u32_e32 v54, 3072, v0
	v_lshl_add_u32 v54, v54, 1, 0
	v_cmp_gt_i32_e32 vcc, s33, v54
	v_mov_b32_e32 v56, v40
	v_cmp_gt_u32_e64 s[4:5], s14, v56
	s_and_b64 vcc, vcc, s[4:5]
	v_lshlrev_b32_e32 v56, 3, v56
	s_and_saveexec_b64 s[4:5], vcc
	ds_write_b64 v56, v[14:15] offset:16448
	s_or_b64 exec, exec, s[4:5]
	v_add_u32_e32 v54, 3072, v0
	v_lshl_add_u32 v54, v54, 1, 1
	v_cmp_gt_i32_e32 vcc, s33, v54
	v_mov_b32_e32 v56, v41
	v_cmp_gt_u32_e64 s[4:5], s14, v56
	s_and_b64 vcc, vcc, s[4:5]
	v_lshlrev_b32_e32 v56, 3, v56
	s_and_saveexec_b64 s[4:5], vcc
	ds_write_b64 v56, v[16:17] offset:16448
	s_or_b64 exec, exec, s[4:5]
	v_add_u32_e32 v54, 4096, v0
	v_lshl_add_u32 v54, v54, 1, 0
	v_cmp_gt_i32_e32 vcc, s33, v54
	v_mov_b32_e32 v56, v42
	v_cmp_gt_u32_e64 s[4:5], s14, v56
	s_and_b64 vcc, vcc, s[4:5]
	v_lshlrev_b32_e32 v56, 3, v56
	s_and_saveexec_b64 s[4:5], vcc
	ds_write_b64 v56, v[18:19] offset:16448
	s_or_b64 exec, exec, s[4:5]
	v_add_u32_e32 v54, 4096, v0
	v_lshl_add_u32 v54, v54, 1, 1
	v_cmp_gt_i32_e32 vcc, s33, v54
	v_mov_b32_e32 v56, v43
	v_cmp_gt_u32_e64 s[4:5], s14, v56
	s_and_b64 vcc, vcc, s[4:5]
	v_lshlrev_b32_e32 v56, 3, v56
	s_and_saveexec_b64 s[4:5], vcc
	ds_write_b64 v56, v[20:21] offset:16448
	s_or_b64 exec, exec, s[4:5]
	v_add_u32_e32 v54, 5120, v0
	v_lshl_add_u32 v54, v54, 1, 0
	v_cmp_gt_i32_e32 vcc, s33, v54
	v_mov_b32_e32 v56, v44
	v_cmp_gt_u32_e64 s[4:5], s14, v56
	s_and_b64 vcc, vcc, s[4:5]
	v_lshlrev_b32_e32 v56, 3, v56
	s_and_saveexec_b64 s[4:5], vcc
	ds_write_b64 v56, v[22:23] offset:16448
	s_or_b64 exec, exec, s[4:5]
	v_add_u32_e32 v54, 5120, v0
	v_lshl_add_u32 v54, v54, 1, 1
	v_cmp_gt_i32_e32 vcc, s33, v54
	v_mov_b32_e32 v56, v45
	v_cmp_gt_u32_e64 s[4:5], s14, v56
	s_and_b64 vcc, vcc, s[4:5]
	v_lshlrev_b32_e32 v56, 3, v56
	s_and_saveexec_b64 s[4:5], vcc
	ds_write_b64 v56, v[24:25] offset:16448
	s_or_b64 exec, exec, s[4:5]
	v_add_u32_e32 v54, 6144, v0
	v_lshl_add_u32 v54, v54, 1, 0
	v_cmp_gt_i32_e32 vcc, s33, v54
	v_mov_b32_e32 v56, v46
	v_cmp_gt_u32_e64 s[4:5], s14, v56
	s_and_b64 vcc, vcc, s[4:5]
	v_lshlrev_b32_e32 v56, 3, v56
	s_and_saveexec_b64 s[4:5], vcc
	ds_write_b64 v56, v[26:27] offset:16448
	s_or_b64 exec, exec, s[4:5]
	v_add_u32_e32 v54, 6144, v0
	v_lshl_add_u32 v54, v54, 1, 1
	v_cmp_gt_i32_e32 vcc, s33, v54
	v_mov_b32_e32 v56, v47
	v_cmp_gt_u32_e64 s[4:5], s14, v56
	s_and_b64 vcc, vcc, s[4:5]
	v_lshlrev_b32_e32 v56, 3, v56
	s_and_saveexec_b64 s[4:5], vcc
	ds_write_b64 v56, v[28:29] offset:16448
	s_or_b64 exec, exec, s[4:5]
	v_add_u32_e32 v54, 7168, v0
	v_lshl_add_u32 v54, v54, 1, 0
	v_cmp_gt_i32_e32 vcc, s33, v54
	v_mov_b32_e32 v56, v48
	v_cmp_gt_u32_e64 s[4:5], s14, v56
	s_and_b64 vcc, vcc, s[4:5]
	v_lshlrev_b32_e32 v56, 3, v56
	s_and_saveexec_b64 s[4:5], vcc
	ds_write_b64 v56, v[30:31] offset:16448
	s_or_b64 exec, exec, s[4:5]
	v_add_u32_e32 v54, 7168, v0
	v_lshl_add_u32 v54, v54, 1, 1
	v_cmp_gt_i32_e32 vcc, s33, v54
	v_mov_b32_e32 v56, v49
	v_cmp_gt_u32_e64 s[4:5], s14, v56
	s_and_b64 vcc, vcc, s[4:5]
	v_lshlrev_b32_e32 v56, 3, v56
	s_and_saveexec_b64 s[4:5], vcc
	ds_write_b64 v56, v[32:33] offset:16448
	s_or_b64 exec, exec, s[4:5]
	s_waitcnt lgkmcnt(0)
	s_barrier
	s_sub_i32 s6, s33, 0
	s_min_i32 s6, s6, 8000
	v_lshlrev_b32_e32 v59, 1, v0
	v_cmp_gt_i32_e32 vcc, s6, v59
	s_and_saveexec_b64 s[10:11], vcc
	s_cbranch_execz .Ll2_cpdone0
	v_add_u32_e32 v56, s36, v59
	v_ashrrev_i32_e32 v57, 31, v56
	v_lshl_add_u64 v[56:57], v[56:57], 3, s[40:41]
	v_lshlrev_b32_e32 v58, 4, v0
	s_mov_b64 s[4:5], 0
	s_mov_b64 s[12:13], 0x4000
.Ll2_copy0:
	ds_read_b128 v[60:63], v58 offset:16448
	v_add_u32_e32 v55, 1, v59
	v_cmp_gt_i32_e32 vcc, s6, v55
	s_waitcnt lgkmcnt(0)
	s_mov_b64 s[16:17], exec
	s_and_b64 exec, s[16:17], vcc
	global_store_dwordx4 v[56:57], v[60:63], off
	s_andn2_b64 exec, s[16:17], vcc
	global_store_dwordx2 v[56:57], v[60:61], off
	s_mov_b64 exec, s[16:17]
	v_add_u32_e32 v59, 0x800, v59
	v_cmp_le_i32_e32 vcc, s6, v59
	v_add_u32_e32 v58, 0x4000, v58
	s_or_b64 s[4:5], vcc, s[4:5]
	v_lshl_add_u64 v[56:57], v[56:57], 0, s[12:13]
	s_andn2_b64 exec, exec, s[4:5]
	s_cbranch_execnz .Ll2_copy0
.Ll2_cpdone0:
	s_mov_b64 exec, s[10:11]
	s_cmpk_le_i32 s33, 8000
	s_cbranch_scc1 .LBB3_141
	s_barrier
	v_add_u32_e32 v54, 0, v0
	v_lshl_add_u32 v54, v54, 1, 0
	v_cmp_gt_i32_e32 vcc, s33, v54
	v_subrev_u32_e32 v56, 8000, v34
	v_cmp_gt_u32_e64 s[4:5], s14, v56
	s_and_b64 vcc, vcc, s[4:5]
	v_lshlrev_b32_e32 v56, 3, v56
	s_and_saveexec_b64 s[4:5], vcc
	ds_write_b64 v56, v[2:3] offset:16448
	s_or_b64 exec, exec, s[4:5]
	v_add_u32_e32 v54, 0, v0
	v_lshl_add_u32 v54, v54, 1, 1
	v_cmp_gt_i32_e32 vcc, s33, v54
	v_subrev_u32_e32 v56, 8000, v35
	v_cmp_gt_u32_e64 s[4:5], s14, v56
	s_and_b64 vcc, vcc, s[4:5]
	v_lshlrev_b32_e32 v56, 3, v56
	s_and_saveexec_b64 s[4:5], vcc
	ds_write_b64 v56, v[4:5] offset:16448
	s_or_b64 exec, exec, s[4:5]
	v_add_u32_e32 v54, 1024, v0
	v_lshl_add_u32 v54, v54, 1, 0
	v_cmp_gt_i32_e32 vcc, s33, v54
	v_subrev_u32_e32 v56, 8000, v36
	v_cmp_gt_u32_e64 s[4:5], s14, v56
	s_and_b64 vcc, vcc, s[4:5]
	v_lshlrev_b32_e32 v56, 3, v56
	s_and_saveexec_b64 s[4:5], vcc
	ds_write_b64 v56, v[6:7] offset:16448
	s_or_b64 exec, exec, s[4:5]
	v_add_u32_e32 v54, 1024, v0
	v_lshl_add_u32 v54, v54, 1, 1
	v_cmp_gt_i32_e32 vcc, s33, v54
	v_subrev_u32_e32 v56, 8000, v37
	v_cmp_gt_u32_e64 s[4:5], s14, v56
	s_and_b64 vcc, vcc, s[4:5]
	v_lshlrev_b32_e32 v56, 3, v56
	s_and_saveexec_b64 s[4:5], vcc
	ds_write_b64 v56, v[8:9] offset:16448
	s_or_b64 exec, exec, s[4:5]
	v_add_u32_e32 v54, 2048, v0
	v_lshl_add_u32 v54, v54, 1, 0
	v_cmp_gt_i32_e32 vcc, s33, v54
	v_subrev_u32_e32 v56, 8000, v38
	v_cmp_gt_u32_e64 s[4:5], s14, v56
	s_and_b64 vcc, vcc, s[4:5]
	v_lshlrev_b32_e32 v56, 3, v56
	s_and_saveexec_b64 s[4:5], vcc
	ds_write_b64 v56, v[10:11] offset:16448
	s_or_b64 exec, exec, s[4:5]
	v_add_u32_e32 v54, 2048, v0
	v_lshl_add_u32 v54, v54, 1, 1
	v_cmp_gt_i32_e32 vcc, s33, v54
	v_subrev_u32_e32 v56, 8000, v39
	v_cmp_gt_u32_e64 s[4:5], s14, v56
	s_and_b64 vcc, vcc, s[4:5]
	v_lshlrev_b32_e32 v56, 3, v56
	s_and_saveexec_b64 s[4:5], vcc
	ds_write_b64 v56, v[12:13] offset:16448
	s_or_b64 exec, exec, s[4:5]
	v_add_u32_e32 v54, 3072, v0
	v_lshl_add_u32 v54, v54, 1, 0
	v_cmp_gt_i32_e32 vcc, s33, v54
	v_subrev_u32_e32 v56, 8000, v40
	v_cmp_gt_u32_e64 s[4:5], s14, v56
	s_and_b64 vcc, vcc, s[4:5]
	v_lshlrev_b32_e32 v56, 3, v56
	s_and_saveexec_b64 s[4:5], vcc
	ds_write_b64 v56, v[14:15] offset:16448
	s_or_b64 exec, exec, s[4:5]
	v_add_u32_e32 v54, 3072, v0
	v_lshl_add_u32 v54, v54, 1, 1
	v_cmp_gt_i32_e32 vcc, s33, v54
	v_subrev_u32_e32 v56, 8000, v41
	v_cmp_gt_u32_e64 s[4:5], s14, v56
	s_and_b64 vcc, vcc, s[4:5]
	v_lshlrev_b32_e32 v56, 3, v56
	s_and_saveexec_b64 s[4:5], vcc
	ds_write_b64 v56, v[16:17] offset:16448
	s_or_b64 exec, exec, s[4:5]
	v_add_u32_e32 v54, 4096, v0
	v_lshl_add_u32 v54, v54, 1, 0
	v_cmp_gt_i32_e32 vcc, s33, v54
	v_subrev_u32_e32 v56, 8000, v42
	v_cmp_gt_u32_e64 s[4:5], s14, v56
	s_and_b64 vcc, vcc, s[4:5]
	v_lshlrev_b32_e32 v56, 3, v56
	s_and_saveexec_b64 s[4:5], vcc
	ds_write_b64 v56, v[18:19] offset:16448
	s_or_b64 exec, exec, s[4:5]
	v_add_u32_e32 v54, 4096, v0
	v_lshl_add_u32 v54, v54, 1, 1
	v_cmp_gt_i32_e32 vcc, s33, v54
	v_subrev_u32_e32 v56, 8000, v43
	v_cmp_gt_u32_e64 s[4:5], s14, v56
	s_and_b64 vcc, vcc, s[4:5]
	v_lshlrev_b32_e32 v56, 3, v56
	s_and_saveexec_b64 s[4:5], vcc
	ds_write_b64 v56, v[20:21] offset:16448
	s_or_b64 exec, exec, s[4:5]
	v_add_u32_e32 v54, 5120, v0
	v_lshl_add_u32 v54, v54, 1, 0
	v_cmp_gt_i32_e32 vcc, s33, v54
	v_subrev_u32_e32 v56, 8000, v44
	v_cmp_gt_u32_e64 s[4:5], s14, v56
	s_and_b64 vcc, vcc, s[4:5]
	v_lshlrev_b32_e32 v56, 3, v56
	s_and_saveexec_b64 s[4:5], vcc
	ds_write_b64 v56, v[22:23] offset:16448
	s_or_b64 exec, exec, s[4:5]
	v_add_u32_e32 v54, 5120, v0
	v_lshl_add_u32 v54, v54, 1, 1
	v_cmp_gt_i32_e32 vcc, s33, v54
	v_subrev_u32_e32 v56, 8000, v45
	v_cmp_gt_u32_e64 s[4:5], s14, v56
	s_and_b64 vcc, vcc, s[4:5]
	v_lshlrev_b32_e32 v56, 3, v56
	s_and_saveexec_b64 s[4:5], vcc
	ds_write_b64 v56, v[24:25] offset:16448
	s_or_b64 exec, exec, s[4:5]
	v_add_u32_e32 v54, 6144, v0
	v_lshl_add_u32 v54, v54, 1, 0
	v_cmp_gt_i32_e32 vcc, s33, v54
	v_subrev_u32_e32 v56, 8000, v46
	v_cmp_gt_u32_e64 s[4:5], s14, v56
	s_and_b64 vcc, vcc, s[4:5]
	v_lshlrev_b32_e32 v56, 3, v56
	s_and_saveexec_b64 s[4:5], vcc
	ds_write_b64 v56, v[26:27] offset:16448
	s_or_b64 exec, exec, s[4:5]
	v_add_u32_e32 v54, 6144, v0
	v_lshl_add_u32 v54, v54, 1, 1
	v_cmp_gt_i32_e32 vcc, s33, v54
	v_subrev_u32_e32 v56, 8000, v47
	v_cmp_gt_u32_e64 s[4:5], s14, v56
	s_and_b64 vcc, vcc, s[4:5]
	v_lshlrev_b32_e32 v56, 3, v56
	s_and_saveexec_b64 s[4:5], vcc
	ds_write_b64 v56, v[28:29] offset:16448
	s_or_b64 exec, exec, s[4:5]
	v_add_u32_e32 v54, 7168, v0
	v_lshl_add_u32 v54, v54, 1, 0
	v_cmp_gt_i32_e32 vcc, s33, v54
	v_subrev_u32_e32 v56, 8000, v48
	v_cmp_gt_u32_e64 s[4:5], s14, v56
	s_and_b64 vcc, vcc, s[4:5]
	v_lshlrev_b32_e32 v56, 3, v56
	s_and_saveexec_b64 s[4:5], vcc
	ds_write_b64 v56, v[30:31] offset:16448
	s_or_b64 exec, exec, s[4:5]
	v_add_u32_e32 v54, 7168, v0
	v_lshl_add_u32 v54, v54, 1, 1
	v_cmp_gt_i32_e32 vcc, s33, v54
	v_subrev_u32_e32 v56, 8000, v49
	v_cmp_gt_u32_e64 s[4:5], s14, v56
	s_and_b64 vcc, vcc, s[4:5]
	v_lshlrev_b32_e32 v56, 3, v56
	s_and_saveexec_b64 s[4:5], vcc
	ds_write_b64 v56, v[32:33] offset:16448
	s_or_b64 exec, exec, s[4:5]
	s_waitcnt lgkmcnt(0)
	s_barrier
	s_sub_i32 s6, s33, 8000
	s_min_i32 s6, s6, 8000
	v_lshlrev_b32_e32 v59, 1, v0
	v_cmp_gt_i32_e32 vcc, s6, v59
	s_and_saveexec_b64 s[10:11], vcc
	s_cbranch_execz .Ll2_cpdone1
	v_add_u32_e32 v56, s36, v59
	v_add_u32_e32 v56, 8000, v56
	v_ashrrev_i32_e32 v57, 31, v56
	v_lshl_add_u64 v[56:57], v[56:57], 3, s[40:41]
	v_lshlrev_b32_e32 v58, 4, v0
	s_mov_b64 s[4:5], 0
	s_mov_b64 s[12:13], 0x4000

.Ll2_cpdone1:
	s_mov_b64 exec, s[10:11]

	.amdhsa_kernel _Z4k_l2PK15HIP_vector_typeIiLj2EEPKiPiPS0_ii
		.amdhsa_group_segment_fixed_size 80448
		.amdhsa_private_segment_fixed_size 0
		.amdhsa_kernarg_size 296
		.amdhsa_user_sgpr_count 2
		.amdhsa_user_sgpr_dispatch_ptr 0
		.amdhsa_user_sgpr_queue_ptr 0
		.amdhsa_user_sgpr_kernarg_segment_ptr 1
		.amdhsa_user_sgpr_dispatch_id 0
		.amdhsa_user_sgpr_kernarg_preload_length 0
		.amdhsa_user_sgpr_kernarg_preload_offset 0
		.amdhsa_user_sgpr_private_segment_size 0
		.amdhsa_uses_dynamic_stack 0
		.amdhsa_enable_private_segment 0
		.amdhsa_system_sgpr_workgroup_id_x 1
		.amdhsa_system_sgpr_workgroup_id_y 0
		.amdhsa_system_sgpr_workgroup_id_z 0
		.amdhsa_system_sgpr_workgroup_info 0
		.amdhsa_system_vgpr_workitem_id 0
		.amdhsa_next_free_vgpr 64
		.amdhsa_next_free_sgpr 48
		.amdhsa_accum_offset 64
		.amdhsa_reserve_vcc 1
		.amdhsa_float_round_mode_32 0
		.amdhsa_float_round_mode_16_64 0
		.amdhsa_float_denorm_mode_32 3
		.amdhsa_float_denorm_mode_16_64 3
		.amdhsa_dx10_clamp 1
		.amdhsa_ieee_mode 1
		.amdhsa_fp16_overflow 0
		.amdhsa_tg_split 0
		.amdhsa_exception_fp_ieee_invalid_op 0
		.amdhsa_exception_fp_denorm_src 0
		.amdhsa_exception_fp_ieee_div_zero 0
		.amdhsa_exception_fp_ieee_overflow 0
		.amdhsa_exception_fp_ieee_underflow 0
		.amdhsa_exception_fp_ieee_inexact 0
		.amdhsa_exception_int_div_zero 0
	.end_amdhsa_kernel

amdhsa.kernels:
  - .agpr_count:     0
    .args:
      - .actual_access:  read_only
        .address_space:  global
        .offset:         0
        .size:           8
        .value_kind:     global_buffer
      - .actual_access:  write_only
        .address_space:  global
        .offset:         8
        .size:           8
        .value_kind:     global_buffer
      - .offset:         16
        .size:           4
        .value_kind:     by_value
      - .offset:         20
        .size:           4
        .value_kind:     by_value
    .group_segment_fixed_size: 8192
    .kernarg_segment_align: 8
    .kernarg_segment_size: 24
    .language:       OpenCL C
    .language_version:
      - 2
      - 0
    .max_flat_workgroup_size: 1024
    .name:           _Z7k_bhistPKiPiii
    .private_segment_fixed_size: 0
    .sgpr_count:     24
    .sgpr_spill_count: 0
    .symbol:         _Z7k_bhistPKiPiii.kd
    .uniform_work_group_size: 1
    .uses_dynamic_stack: false
    .vgpr_count:     50
    .vgpr_spill_count: 0
    .wavefront_size: 64
  - .agpr_count:     0
    .args:
      - .address_space:  global
        .offset:         0
        .size:           8
        .value_kind:     global_buffer
      - .actual_access:  write_only
        .address_space:  global
        .offset:         8
        .size:           8
        .value_kind:     global_buffer
      - .offset:         16
        .size:           4
        .value_kind:     by_value
      - .offset:         20
        .size:           4
        .value_kind:     by_value
      - .offset:         24
        .size:           4
        .value_kind:     by_value
      - .actual_access:  read_only
        .address_space:  global
        .offset:         32
        .size:           8
        .value_kind:     global_buffer
      - .actual_access:  read_only
        .address_space:  global
        .offset:         40
        .size:           8
        .value_kind:     global_buffer
      - .offset:         48
        .size:           4
        .value_kind:     by_value
      - .offset:         52
        .size:           4
        .value_kind:     by_value
      - .actual_access:  write_only
        .address_space:  global
        .offset:         56
        .size:           8
        .value_kind:     global_buffer
      - .actual_access:  write_only
        .address_space:  global
        .offset:         64
        .size:           8
        .value_kind:     global_buffer
      - .actual_access:  write_only
        .address_space:  global
        .offset:         72
        .size:           8
        .value_kind:     global_buffer
    .group_segment_fixed_size: 4160
    .kernarg_segment_align: 8
    .kernarg_segment_size: 80
    .language:       OpenCL C
    .language_version:
      - 2
      - 0
    .max_flat_workgroup_size: 1024
    .name:           _Z12k_bscan_prepPiS_iiiPKfS1_iiPDF16_PfS3_
    .private_segment_fixed_size: 0
    .sgpr_count:     24
    .sgpr_spill_count: 0
    .symbol:         _Z12k_bscan_prepPiS_iiiPKfS1_iiPDF16_PfS3_.kd
    .uniform_work_group_size: 1
    .uses_dynamic_stack: false
    .vgpr_count:     28
    .vgpr_spill_count: 0
    .wavefront_size: 64
  - .agpr_count:     0
    .args:
      - .actual_access:  read_only
        .address_space:  global
        .offset:         0
        .size:           8
        .value_kind:     global_buffer
      - .actual_access:  read_only
        .address_space:  global
        .offset:         8
        .size:           8
        .value_kind:     global_buffer
      - .actual_access:  read_only
        .address_space:  global
        .offset:         16
        .size:           8
        .value_kind:     global_buffer
      - .actual_access:  read_only
        .address_space:  global
        .offset:         24
        .size:           8
        .value_kind:     global_buffer
      - .actual_access:  read_only
        .address_space:  global
        .offset:         32
        .size:           8
        .value_kind:     global_buffer
      - .actual_access:  write_only
        .address_space:  global
        .offset:         40
        .size:           8
        .value_kind:     global_buffer
      - .actual_access:  write_only
        .address_space:  global
        .offset:         48
        .size:           8
        .value_kind:     global_buffer
      - .offset:         56
        .size:           4
        .value_kind:     by_value
      - .offset:         60
        .size:           4
        .value_kind:     by_value
      - .offset:         64
        .size:           4
        .value_kind:     by_value
      - .offset:         72
        .size:           4
        .value_kind:     hidden_block_count_x
      - .offset:         76
        .size:           4
        .value_kind:     hidden_block_count_y
      - .offset:         80
        .size:           4
        .value_kind:     hidden_block_count_z
      - .offset:         84
        .size:           2
        .value_kind:     hidden_group_size_x
      - .offset:         86
        .size:           2
        .value_kind:     hidden_group_size_y
      - .offset:         88
        .size:           2
        .value_kind:     hidden_group_size_z
      - .offset:         90
        .size:           2
        .value_kind:     hidden_remainder_x
      - .offset:         92
        .size:           2
        .value_kind:     hidden_remainder_y
      - .offset:         94
        .size:           2
        .value_kind:     hidden_remainder_z
      - .offset:         112
        .size:           8
        .value_kind:     hidden_global_offset_x
      - .offset:         120
        .size:           8
        .value_kind:     hidden_global_offset_y
      - .offset:         128
        .size:           8
        .value_kind:     hidden_global_offset_z
      - .offset:         136
        .size:           2
        .value_kind:     hidden_grid_dims
    .group_segment_fixed_size: 154816
    .kernarg_segment_align: 8
    .kernarg_segment_size: 328
    .language:       OpenCL C
    .language_version:
      - 2
      - 0
    .max_flat_workgroup_size: 1024
    .name:           _Z4k_l1PKiS0_PKfS0_S0_PiP15HIP_vector_typeIiLj2EEiii
    .private_segment_fixed_size: 0
    .sgpr_count:     92
    .sgpr_spill_count: 0
    .symbol:         _Z4k_l1PKiS0_PKfS0_S0_PiP15HIP_vector_typeIiLj2EEiii.kd
    .uniform_work_group_size: 1
    .uses_dynamic_stack: false
    .vgpr_count:     128
    .vgpr_spill_count: 0
    .wavefront_size: 64
  - .agpr_count:     0
    .args:
      - .actual_access:  read_only
        .address_space:  global
        .offset:         0
        .size:           8
        .value_kind:     global_buffer
      - .actual_access:  read_only
        .address_space:  global
        .offset:         8
        .size:           8
        .value_kind:     global_buffer
      - .actual_access:  write_only
        .address_space:  global
        .offset:         16
        .size:           8
        .value_kind:     global_buffer
      - .actual_access:  write_only
        .address_space:  global
        .offset:         24
        .size:           8
        .value_kind:     global_buffer
      - .offset:         32
        .size:           4
        .value_kind:     by_value
      - .offset:         36
        .size:           4
        .value_kind:     by_value
      - .offset:         40
        .size:           4
        .value_kind:     hidden_block_count_x
      - .offset:         44
        .size:           4
        .value_kind:     hidden_block_count_y
      - .offset:         48
        .size:           4
        .value_kind:     hidden_block_count_z
      - .offset:         52
        .size:           2
        .value_kind:     hidden_group_size_x
      - .offset:         54
        .size:           2
        .value_kind:     hidden_group_size_y
      - .offset:         56
        .size:           2
        .value_kind:     hidden_group_size_z
      - .offset:         58
        .size:           2
        .value_kind:     hidden_remainder_x
      - .offset:         60
        .size:           2
        .value_kind:     hidden_remainder_y
      - .offset:         62
        .size:           2
        .value_kind:     hidden_remainder_z
      - .offset:         80
        .size:           8
        .value_kind:     hidden_global_offset_x
      - .offset:         88
        .size:           8
        .value_kind:     hidden_global_offset_y
      - .offset:         96
        .size:           8
        .value_kind:     hidden_global_offset_z
      - .offset:         104
        .size:           2
        .value_kind:     hidden_grid_dims
    .group_segment_fixed_size: 80448
    .kernarg_segment_align: 8
    .kernarg_segment_size: 296
    .language:       OpenCL C
    .language_version:
      - 2
      - 0
    .max_flat_workgroup_size: 1024
    .name:           _Z4k_l2PK15HIP_vector_typeIiLj2EEPKiPiPS0_ii
    .private_segment_fixed_size: 0
    .sgpr_count:     54
    .sgpr_spill_count: 0
    .symbol:         _Z4k_l2PK15HIP_vector_typeIiLj2EEPKiPiPS0_ii.kd
    .uniform_work_group_size: 1
    .uses_dynamic_stack: false
    .vgpr_count:     64
    .vgpr_spill_count: 0
    .wavefront_size: 64
  - .agpr_count:     0
    .args:
      - .actual_access:  read_only
        .address_space:  global
        .offset:         0
        .size:           8
        .value_kind:     global_buffer
      - .actual_access:  read_only
        .address_space:  global
        .offset:         8
        .size:           8
        .value_kind:     global_buffer
      - .actual_access:  read_only
        .address_space:  global
        .offset:         16
        .size:           8
        .value_kind:     global_buffer
      - .actual_access:  read_only
        .address_space:  global
        .offset:         24
        .size:           8
        .value_kind:     global_buffer
      - .actual_access:  read_only
        .address_space:  global
        .offset:         32
        .size:           8
        .value_kind:     global_buffer
      - .actual_access:  read_only
        .address_space:  global
        .offset:         40
        .size:           8
        .value_kind:     global_buffer
      - .actual_access:  read_only
        .address_space:  global
        .offset:         48
        .size:           8
        .value_kind:     global_buffer
      - .offset:         56
        .size:           4
        .value_kind:     by_value
      - .actual_access:  read_only
        .address_space:  global
        .offset:         64
        .size:           8
        .value_kind:     global_buffer
      - .actual_access:  write_only
        .address_space:  global
        .offset:         72
        .size:           8
        .value_kind:     global_buffer
      - .actual_access:  write_only
        .address_space:  global
        .offset:         80
        .size:           8
        .value_kind:     global_buffer
      - .actual_access:  write_only
        .address_space:  global
        .offset:         88
        .size:           8
        .value_kind:     global_buffer
      - .actual_access:  read_only
        .address_space:  global
        .offset:         96
        .size:           8
        .value_kind:     global_buffer
      - .actual_access:  read_only
        .address_space:  global
        .offset:         104
        .size:           8
        .value_kind:     global_buffer
      - .actual_access:  read_only
        .address_space:  global
        .offset:         112
        .size:           8
        .value_kind:     global_buffer
      - .actual_access:  read_only
        .address_space:  global
        .offset:         120
        .size:           8
        .value_kind:     global_buffer
      - .actual_access:  read_only
        .address_space:  global
        .offset:         128
        .size:           8
        .value_kind:     global_buffer
      - .offset:         136
        .size:           4
        .value_kind:     by_value
      - .offset:         144
        .size:           4
        .value_kind:     hidden_block_count_x
      - .offset:         148
        .size:           4
        .value_kind:     hidden_block_count_y
      - .offset:         152
        .size:           4
        .value_kind:     hidden_block_count_z
      - .offset:         156
        .size:           2
        .value_kind:     hidden_group_size_x
      - .offset:         158
        .size:           2
        .value_kind:     hidden_group_size_y
      - .offset:         160
        .size:           2
        .value_kind:     hidden_group_size_z
      - .offset:         162
        .size:           2
        .value_kind:     hidden_remainder_x
      - .offset:         164
        .size:           2
        .value_kind:     hidden_remainder_y
      - .offset:         166
        .size:           2
        .value_kind:     hidden_remainder_z
      - .offset:         184
        .size:           8
        .value_kind:     hidden_global_offset_x
      - .offset:         192
        .size:           8
        .value_kind:     hidden_global_offset_y
      - .offset:         200
        .size:           8
        .value_kind:     hidden_global_offset_z
      - .offset:         208
        .size:           2
        .value_kind:     hidden_grid_dims
    .group_segment_fixed_size: 20544
    .kernarg_segment_align: 8
    .kernarg_segment_size: 400
    .language:       OpenCL C
    .language_version:
      - 2
      - 0
    .max_flat_workgroup_size: 512
    .name:           _Z6k_spmmILb0ELi0EEvPKiPK15HIP_vector_typeIiLj2EEPKvPKfPKDF16_S9_S9_iPfPDF16_PhSC_PKhS9_SG_S9_S9_i
    .private_segment_fixed_size: 0
    .sgpr_count:     36
    .sgpr_spill_count: 0
    .symbol:         _Z6k_spmmILb0ELi0EEvPKiPK15HIP_vector_typeIiLj2EEPKvPKfPKDF16_S9_S9_iPfPDF16_PhSC_PKhS9_SG_S9_S9_i.kd
    .uniform_work_group_size: 1
    .uses_dynamic_stack: false
    .vgpr_count:     128
    .vgpr_spill_count: 0
    .wavefront_size: 64
  - .agpr_count:     0
    .args:
      - .actual_access:  read_only
        .address_space:  global
        .offset:         0
        .size:           8
        .value_kind:     global_buffer
      - .actual_access:  read_only
        .address_space:  global
        .offset:         8
        .size:           8
        .value_kind:     global_buffer
      - .actual_access:  read_only
        .address_space:  global
        .offset:         16
        .size:           8
        .value_kind:     global_buffer
      - .actual_access:  read_only
        .address_space:  global
        .offset:         24
        .size:           8
        .value_kind:     global_buffer
      - .actual_access:  read_only
        .address_space:  global
        .offset:         32
        .size:           8
        .value_kind:     global_buffer
      - .actual_access:  read_only
        .address_space:  global
        .offset:         40
        .size:           8
        .value_kind:     global_buffer
      - .actual_access:  read_only
        .address_space:  global
        .offset:         48
        .size:           8
        .value_kind:     global_buffer
      - .offset:         56
        .size:           4
        .value_kind:     by_value
      - .actual_access:  read_only
        .address_space:  global
        .offset:         64
        .size:           8
        .value_kind:     global_buffer
      - .actual_access:  read_only
        .address_space:  global
        .offset:         72
        .size:           8
        .value_kind:     global_buffer
      - .actual_access:  write_only
        .address_space:  global
        .offset:         80
        .size:           8
        .value_kind:     global_buffer
      - .actual_access:  write_only
        .address_space:  global
        .offset:         88
        .size:           8
        .value_kind:     global_buffer
      - .actual_access:  read_only
        .address_space:  global
        .offset:         96
        .size:           8
        .value_kind:     global_buffer
      - .actual_access:  read_only
        .address_space:  global
        .offset:         104
        .size:           8
        .value_kind:     global_buffer
      - .actual_access:  read_only
        .address_space:  global
        .offset:         112
        .size:           8
        .value_kind:     global_buffer
      - .actual_access:  read_only
        .address_space:  global
        .offset:         120
        .size:           8
        .value_kind:     global_buffer
      - .actual_access:  read_only
        .address_space:  global
        .offset:         128
        .size:           8
        .value_kind:     global_buffer
      - .offset:         136
        .size:           4
        .value_kind:     by_value
      - .offset:         144
        .size:           4
        .value_kind:     hidden_block_count_x
      - .offset:         148
        .size:           4
        .value_kind:     hidden_block_count_y
      - .offset:         152
        .size:           4
        .value_kind:     hidden_block_count_z
      - .offset:         156
        .size:           2
        .value_kind:     hidden_group_size_x
      - .offset:         158
        .size:           2
        .value_kind:     hidden_group_size_y
      - .offset:         160
        .size:           2
        .value_kind:     hidden_group_size_z
      - .offset:         162
        .size:           2
        .value_kind:     hidden_remainder_x
      - .offset:         164
        .size:           2
        .value_kind:     hidden_remainder_y
      - .offset:         166
        .size:           2
        .value_kind:     hidden_remainder_z
      - .offset:         184
        .size:           8
        .value_kind:     hidden_global_offset_x
      - .offset:         192
        .size:           8
        .value_kind:     hidden_global_offset_y
      - .offset:         200
        .size:           8
        .value_kind:     hidden_global_offset_z
      - .offset:         208
        .size:           2
        .value_kind:     hidden_grid_dims
    .group_segment_fixed_size: 20544
    .kernarg_segment_align: 8
    .kernarg_segment_size: 400
    .language:       OpenCL C
    .language_version:
      - 2
      - 0
    .max_flat_workgroup_size: 512
    .name:           _Z6k_spmmILb1ELi1EEvPKiPK15HIP_vector_typeIiLj2EEPKvPKfPKDF16_S9_S9_iPfPDF16_PhSC_PKhS9_SG_S9_S9_i
    .private_segment_fixed_size: 0
    .sgpr_count:     36
    .sgpr_spill_count: 0
    .symbol:         _Z6k_spmmILb1ELi1EEvPKiPK15HIP_vector_typeIiLj2EEPKvPKfPKDF16_S9_S9_iPfPDF16_PhSC_PKhS9_SG_S9_S9_i.kd
    .uniform_work_group_size: 1
    .uses_dynamic_stack: false
    .vgpr_count:     64
    .vgpr_spill_count: 0
    .wavefront_size: 64
  - .agpr_count:     0
    .args:
      - .actual_access:  read_only
        .address_space:  global
        .offset:         0
        .size:           8
        .value_kind:     global_buffer
      - .actual_access:  read_only
        .address_space:  global
        .offset:         8
        .size:           8
        .value_kind:     global_buffer
      - .actual_access:  read_only
        .address_space:  global
        .offset:         16
        .size:           8
        .value_kind:     global_buffer
      - .actual_access:  read_only
        .address_space:  global
        .offset:         24
        .size:           8
        .value_kind:     global_buffer
      - .actual_access:  read_only
        .address_space:  global
        .offset:         32
        .size:           8
        .value_kind:     global_buffer
      - .actual_access:  read_only
        .address_space:  global
        .offset:         40
        .size:           8
        .value_kind:     global_buffer
      - .actual_access:  read_only
        .address_space:  global
        .offset:         48
        .size:           8
        .value_kind:     global_buffer
      - .offset:         56
        .size:           4
        .value_kind:     by_value
      - .actual_access:  write_only
        .address_space:  global
        .offset:         64
        .size:           8
        .value_kind:     global_buffer
      - .actual_access:  read_only
        .address_space:  global
        .offset:         72
        .size:           8
        .value_kind:     global_buffer
      - .actual_access:  read_only
        .address_space:  global
        .offset:         80
        .size:           8
        .value_kind:     global_buffer
      - .actual_access:  read_only
        .address_space:  global
        .offset:         88
        .size:           8
        .value_kind:     global_buffer
      - .actual_access:  read_only
        .address_space:  global
        .offset:         96
        .size:           8
        .value_kind:     global_buffer
      - .actual_access:  read_only
        .address_space:  global
        .offset:         104
        .size:           8
        .value_kind:     global_buffer
      - .actual_access:  read_only
        .address_space:  global
        .offset:         112
        .size:           8
        .value_kind:     global_buffer
      - .actual_access:  read_only
        .address_space:  global
        .offset:         120
        .size:           8
        .value_kind:     global_buffer
      - .actual_access:  read_only
        .address_space:  global
        .offset:         128
        .size:           8
        .value_kind:     global_buffer
      - .offset:         136
        .size:           4
        .value_kind:     by_value
      - .offset:         144
        .size:           4
        .value_kind:     hidden_block_count_x
      - .offset:         148
        .size:           4
        .value_kind:     hidden_block_count_y
      - .offset:         152
        .size:           4
        .value_kind:     hidden_block_count_z
      - .offset:         156
        .size:           2
        .value_kind:     hidden_group_size_x
      - .offset:         158
        .size:           2
        .value_kind:     hidden_group_size_y
      - .offset:         160
        .size:           2
        .value_kind:     hidden_group_size_z
      - .offset:         162
        .size:           2
        .value_kind:     hidden_remainder_x
      - .offset:         164
        .size:           2
        .value_kind:     hidden_remainder_y
      - .offset:         166
        .size:           2
        .value_kind:     hidden_remainder_z
      - .offset:         184
        .size:           8
        .value_kind:     hidden_global_offset_x
      - .offset:         192
        .size:           8
        .value_kind:     hidden_global_offset_y
      - .offset:         200
        .size:           8
        .value_kind:     hidden_global_offset_z
      - .offset:         208
        .size:           2
        .value_kind:     hidden_grid_dims
    .group_segment_fixed_size: 20480
    .kernarg_segment_align: 8
    .kernarg_segment_size: 400
    .language:       OpenCL C
    .language_version:
      - 2
      - 0
    .max_flat_workgroup_size: 512
    .name:           _Z6k_spmmILb1ELi2EEvPKiPK15HIP_vector_typeIiLj2EEPKvPKfPKDF16_S9_S9_iPfPDF16_PhSC_PKhS9_SG_S9_S9_i
    .private_segment_fixed_size: 0
    .sgpr_count:     42
    .sgpr_spill_count: 0
    .symbol:         _Z6k_spmmILb1ELi2EEvPKiPK15HIP_vector_typeIiLj2EEPKvPKfPKDF16_S9_S9_iPfPDF16_PhSC_PKhS9_SG_S9_S9_i.kd
    .uniform_work_group_size: 1
    .uses_dynamic_stack: false
    .vgpr_count:     64
    .vgpr_spill_count: 0
    .wavefront_size: 64
